# P0 ada GEMV: silu(c) staging loop unrolled with all 8 loads in flight (counted waits)
# baseline (speedup 1.0000x reference)
.LBB0_12:
	global_load_dword v16, v[12:13], off
	global_load_dword v17, v[10:11], off
	global_load_dword v90, v[12:13], off offset:2048
	global_load_dword v91, v[10:11], off offset:2048
	v_lshl_add_u64 v[12:13], v[12:13], 0, s[14:15]
	v_lshl_add_u64 v[12:13], v[12:13], 0, s[14:15]
	v_lshl_add_u64 v[10:11], v[10:11], 0, s[14:15]
	v_lshl_add_u64 v[10:11], v[10:11], 0, s[14:15]
	global_load_dword v92, v[12:13], off
	global_load_dword v93, v[10:11], off
	global_load_dword v94, v[12:13], off offset:2048
	global_load_dword v95, v[10:11], off offset:2048
	s_waitcnt vmcnt(7)
	v_mul_f32_e32 v18, 0xbfb8aa3b, v16
	s_waitcnt vmcnt(6)
	v_mul_f32_e32 v19, 0xbfb8aa3b, v17
	v_exp_f32_e32 v18, v18
	v_exp_f32_e32 v19, v19
	v_add_f32_e32 v18, 1.0, v18
	v_add_f32_e32 v19, 1.0, v19
	v_div_scale_f32 v20, s[2:3], v18, v18, v16
	v_div_scale_f32 v22, s[2:3], v19, v19, v17
	v_rcp_f32_e32 v24, v20
	v_rcp_f32_e32 v25, v22
	v_div_scale_f32 v21, vcc, v16, v18, v16
	v_fma_f32 v26, -v20, v24, 1.0
	v_fma_f32 v27, -v22, v25, 1.0
	v_fmac_f32_e32 v24, v26, v24
	v_div_scale_f32 v23, s[2:3], v17, v19, v17
	v_fmac_f32_e32 v25, v27, v25
	v_mul_f32_e32 v26, v21, v24
	v_mul_f32_e32 v27, v23, v25
	v_fma_f32 v28, -v20, v26, v21
	v_fma_f32 v29, -v22, v27, v23
	v_fmac_f32_e32 v26, v28, v24
	v_fmac_f32_e32 v27, v29, v25
	v_fma_f32 v20, -v20, v26, v21
	v_fma_f32 v21, -v22, v27, v23
	v_div_fmas_f32 v20, v20, v24, v26
	s_mov_b64 vcc, s[2:3]
	v_div_fixup_f32 v16, v20, v18, v16
	v_div_fmas_f32 v18, v21, v25, v27
	v_div_fixup_f32 v17, v18, v19, v17
	ds_write2st64_b32 v9, v16, v17 offset0:0 offset1:32
	s_waitcnt vmcnt(5)
	v_mul_f32_e32 v18, 0xbfb8aa3b, v90
	s_waitcnt vmcnt(4)
	v_mul_f32_e32 v19, 0xbfb8aa3b, v91
	v_exp_f32_e32 v18, v18
	v_exp_f32_e32 v19, v19
	v_add_f32_e32 v18, 1.0, v18
	v_add_f32_e32 v19, 1.0, v19
	v_div_scale_f32 v20, s[2:3], v18, v18, v90
	v_div_scale_f32 v22, s[2:3], v19, v19, v91
	v_rcp_f32_e32 v24, v20
	v_rcp_f32_e32 v25, v22
	v_div_scale_f32 v21, vcc, v90, v18, v90
	v_fma_f32 v26, -v20, v24, 1.0
	v_fma_f32 v27, -v22, v25, 1.0
	v_fmac_f32_e32 v24, v26, v24
	v_div_scale_f32 v23, s[2:3], v91, v19, v91
	v_fmac_f32_e32 v25, v27, v25
	v_mul_f32_e32 v26, v21, v24
	v_mul_f32_e32 v27, v23, v25
	v_fma_f32 v28, -v20, v26, v21
	v_fma_f32 v29, -v22, v27, v23
	v_fmac_f32_e32 v26, v28, v24
	v_fmac_f32_e32 v27, v29, v25
	v_fma_f32 v20, -v20, v26, v21
	v_fma_f32 v21, -v22, v27, v23
	v_div_fmas_f32 v20, v20, v24, v26
	s_mov_b64 vcc, s[2:3]
	v_div_fixup_f32 v90, v20, v18, v90
	v_div_fmas_f32 v18, v21, v25, v27
	v_div_fixup_f32 v91, v18, v19, v91
	ds_write2st64_b32 v9, v90, v91 offset0:8 offset1:40
	s_waitcnt vmcnt(3)
	v_mul_f32_e32 v18, 0xbfb8aa3b, v92
	s_waitcnt vmcnt(2)
	v_mul_f32_e32 v19, 0xbfb8aa3b, v93
	v_exp_f32_e32 v18, v18
	v_exp_f32_e32 v19, v19
	v_add_f32_e32 v18, 1.0, v18
	v_add_f32_e32 v19, 1.0, v19
	v_div_scale_f32 v20, s[2:3], v18, v18, v92
	v_div_scale_f32 v22, s[2:3], v19, v19, v93
	v_rcp_f32_e32 v24, v20
	v_rcp_f32_e32 v25, v22
	v_div_scale_f32 v21, vcc, v92, v18, v92
	v_fma_f32 v26, -v20, v24, 1.0
	v_fma_f32 v27, -v22, v25, 1.0
	v_fmac_f32_e32 v24, v26, v24
	v_div_scale_f32 v23, s[2:3], v93, v19, v93
	v_fmac_f32_e32 v25, v27, v25
	v_mul_f32_e32 v26, v21, v24
	v_mul_f32_e32 v27, v23, v25
	v_fma_f32 v28, -v20, v26, v21
	v_fma_f32 v29, -v22, v27, v23
	v_fmac_f32_e32 v26, v28, v24
	v_fmac_f32_e32 v27, v29, v25
	v_fma_f32 v20, -v20, v26, v21
	v_fma_f32 v21, -v22, v27, v23
	v_div_fmas_f32 v20, v20, v24, v26
	s_mov_b64 vcc, s[2:3]
	v_div_fixup_f32 v92, v20, v18, v92
	v_div_fmas_f32 v18, v21, v25, v27
	v_div_fixup_f32 v93, v18, v19, v93
	ds_write2st64_b32 v9, v92, v93 offset0:16 offset1:48
	s_waitcnt vmcnt(1)
	v_mul_f32_e32 v18, 0xbfb8aa3b, v94
	s_waitcnt vmcnt(0)
	v_mul_f32_e32 v19, 0xbfb8aa3b, v95
	v_exp_f32_e32 v18, v18
	v_exp_f32_e32 v19, v19
	v_add_f32_e32 v18, 1.0, v18
	v_add_f32_e32 v19, 1.0, v19
	v_div_scale_f32 v20, s[2:3], v18, v18, v94
	v_div_scale_f32 v22, s[2:3], v19, v19, v95
	v_rcp_f32_e32 v24, v20
	v_rcp_f32_e32 v25, v22
	v_div_scale_f32 v21, vcc, v94, v18, v94
	v_fma_f32 v26, -v20, v24, 1.0
	v_fma_f32 v27, -v22, v25, 1.0
	v_fmac_f32_e32 v24, v26, v24
	v_div_scale_f32 v23, s[2:3], v95, v19, v95
	v_fmac_f32_e32 v25, v27, v25
	v_mul_f32_e32 v26, v21, v24
	v_mul_f32_e32 v27, v23, v25
	v_fma_f32 v28, -v20, v26, v21
	v_fma_f32 v29, -v22, v27, v23
	v_fmac_f32_e32 v26, v28, v24
	v_fmac_f32_e32 v27, v29, v25
	v_fma_f32 v20, -v20, v26, v21
	v_fma_f32 v21, -v22, v27, v23
	v_div_fmas_f32 v20, v20, v24, v26
	s_mov_b64 vcc, s[2:3]
	v_div_fixup_f32 v94, v20, v18, v94
	v_div_fmas_f32 v18, v21, v25, v27
	v_div_fixup_f32 v95, v18, v19, v95
	ds_write2st64_b32 v9, v94, v95 offset0:24 offset1:56
	v_ashrrev_i32_e32 v9, 31, v8
	v_mov_b32_e32 v12, 0
	v_lshl_add_u64 v[10:11], v[8:9], 2, s[12:13]
	s_mov_b32 s2, s24
	s_mov_b32 s3, s23
	v_mov_b32_e32 v13, v12
	s_waitcnt lgkmcnt(0)
	s_barrier
